# baseline (speedup 1.0000x reference)
.LBB0_37:
	s_or_b64 exec, exec, s[0:1]
	v_mov_b32_e32 v98, v97
	v_mov_b32_e32 v99, v97
	v_mov_b32_e32 v5, v97
	v_mov_b32_e32 v6, v97
	v_mov_b32_e32 v7, v97
	v_mov_b32_e32 v1, v97
	v_mov_b32_e32 v2, v97
	v_mov_b32_e32 v3, v97
	s_mov_b32 s0, 0x10000
	v_or_b32_e32 v8, 0x21000, v223
	v_mfma_f32_32x32x16_f16 v[32:47], v[96:99], v[0:3], 0
	v_mfma_f32_32x32x16_f16 v[16:31], v[4:7], v[0:3], 0
	v_or_b32_e32 v114, 0x21000, v223
	v_cmp_eq_u32_e64 s[0:1], 0, v225
	s_and_b64 vcc, vcc, s[0:1]
	ds_read_b128 v[8:11], v114
	ds_read_b128 v[12:15], v114 offset:32
	ds_read_b128 v[234:237], v114 offset:64
	ds_read_b128 v[238:241], v114 offset:96
	ds_read_b128 v[242:245], v114 offset:128
	ds_read_b128 v[106:109], v114 offset:160
	ds_read_b128 v[110:113], v114 offset:192
	s_waitcnt lgkmcnt(7)
	v_mfma_f32_32x32x16_f16 v[32:47], v[180:183], v[92:95], v[32:47]
	ds_read_b128 v[0:3], v114 offset:224
	v_mfma_f32_32x32x16_f16 v[32:47], v[184:187], v[88:91], v[32:47]
	v_mfma_f32_32x32x16_f16 v[32:47], v[188:191], v[84:87], v[32:47]
	v_mfma_f32_32x32x16_f16 v[32:47], v[192:195], v[80:83], v[32:47]
	v_mfma_f32_32x32x16_f16 v[32:47], v[196:199], v[76:79], v[32:47]
	v_mfma_f32_32x32x16_f16 v[32:47], v[200:203], v[72:75], v[32:47]
	v_mfma_f32_32x32x16_f16 v[32:47], v[204:207], v[68:71], v[32:47]
	v_mfma_f32_32x32x16_f16 v[32:47], v[208:211], v[64:67], v[32:47]
	s_waitcnt lgkmcnt(0)
	v_dot2c_f32_f16_e32 v98, v92, v8
	v_mfma_f32_32x32x16_f16 v[16:31], v[148:151], v[92:95], v[16:31]
	v_dot2c_f32_f16_e32 v98, v93, v9
	v_dot2c_f32_f16_e32 v98, v94, v10
	v_dot2c_f32_f16_e32 v98, v95, v11
	v_dot2c_f32_f16_e32 v98, v88, v12
	v_mfma_f32_32x32x16_f16 v[16:31], v[152:155], v[88:91], v[16:31]
	v_dot2c_f32_f16_e32 v98, v89, v13
	v_dot2c_f32_f16_e32 v98, v90, v14
	v_dot2c_f32_f16_e32 v98, v91, v15
	v_dot2c_f32_f16_e32 v98, v84, v234
	v_mfma_f32_32x32x16_f16 v[16:31], v[156:159], v[84:87], v[16:31]
	v_dot2c_f32_f16_e32 v98, v85, v235
	v_dot2c_f32_f16_e32 v98, v86, v236
	v_dot2c_f32_f16_e32 v98, v87, v237
	v_dot2c_f32_f16_e32 v98, v80, v238
	v_mfma_f32_32x32x16_f16 v[16:31], v[160:163], v[80:83], v[16:31]
	v_dot2c_f32_f16_e32 v98, v81, v239
	v_dot2c_f32_f16_e32 v98, v82, v240
	v_dot2c_f32_f16_e32 v98, v83, v241
	v_dot2c_f32_f16_e32 v98, v76, v242
	v_mfma_f32_32x32x16_f16 v[16:31], v[164:167], v[76:79], v[16:31]
	v_dot2c_f32_f16_e32 v98, v77, v243
	v_dot2c_f32_f16_e32 v98, v78, v244
	v_dot2c_f32_f16_e32 v98, v79, v245
	v_dot2c_f32_f16_e32 v98, v72, v106
	v_mfma_f32_32x32x16_f16 v[16:31], v[168:171], v[72:75], v[16:31]
	v_dot2c_f32_f16_e32 v98, v73, v107
	v_dot2c_f32_f16_e32 v98, v74, v108
	v_dot2c_f32_f16_e32 v98, v75, v109
	v_dot2c_f32_f16_e32 v98, v68, v110
	v_mfma_f32_32x32x16_f16 v[16:31], v[172:175], v[68:71], v[16:31]
	v_dot2c_f32_f16_e32 v98, v69, v111
	v_dot2c_f32_f16_e32 v98, v70, v112
	v_dot2c_f32_f16_e32 v98, v71, v113
	v_cvt_pk_f16_f32 v7, v38, v39
	v_cvt_pk_f16_f32 v6, v36, v37
	v_cvt_pk_f16_f32 v5, v34, v35
	v_cvt_pk_f16_f32 v4, v32, v33
	v_dot2c_f32_f16_e32 v98, v64, v0
	v_dot2c_f32_f16_e32 v98, v65, v1
	v_dot2c_f32_f16_e32 v98, v66, v2
	v_mfma_f32_32x32x16_f16 v[16:31], v[176:179], v[64:67], v[16:31]
	v_dot2c_f32_f16_e32 v98, v67, v3
	v_cvt_pk_f16_f32 v35, v46, v47
	v_cvt_pk_f16_f32 v34, v44, v45
	v_cvt_pk_f16_f32 v33, v42, v43
	v_cvt_pk_f16_f32 v32, v40, v41
	ds_bpermute_b32 v36, v102, v98
	v_cvt_f32_i32_e32 v37, v226
	v_mfma_f32_32x32x16_f16 v[0:15], v[4:7], v[60:63], 0
	s_nop 3
	v_cvt_pk_f16_f32 v23, v22, v23
	v_cvt_pk_f16_f32 v22, v20, v21
	v_cvt_pk_f16_f32 v21, v18, v19
	v_cvt_pk_f16_f32 v20, v16, v17
	v_cvt_pk_f16_f32 v19, v30, v31
	v_cvt_pk_f16_f32 v18, v28, v29
	v_cvt_pk_f16_f32 v17, v26, v27
	v_mfma_f32_32x32x16_f16 v[0:15], v[32:35], v[56:59], v[0:15]
	v_cvt_pk_f16_f32 v16, v24, v25
	s_waitcnt lgkmcnt(0)
	v_add_f32_e32 v36, v98, v36
	v_cvt_f16_f32_e32 v26, v100
	v_mov_b32_e32 v98, v97
	v_lshlrev_b32_e32 v32, 4, v218
	v_mfma_f32_32x32x16_f16 v[0:15], v[20:23], v[52:55], v[0:15]
	v_fma_mixlo_f16 v20, v37, v104, v36
	v_pack_b32_f16 v20, v20, 0
	v_pack_b32_f16 v21, v26, 0
	v_cndmask_b32_e32 v96, 0, v21, vcc
	v_mfma_f32_32x32x16_f16 v[0:15], v[16:19], v[48:51], v[0:15]
	v_cndmask_b32_e32 v16, 0, v20, vcc
	v_mov_b32_e32 v17, v97
	v_mov_b32_e32 v18, v97
	v_mov_b32_e32 v19, v97
	v_cmp_ne_u32_e32 vcc, 0, v225
	s_nop 0
	v_mfma_f32_32x32x16_f16 v[0:15], v[16:19], v[96:99], v[0:15]
	v_lshlrev_b32_e32 v70, 2, v215
	v_lshl_add_u32 v70, v214, 4, v70
	global_load_dwordx4 v[16:19], v70, s[64:65]
	global_load_dwordx4 v[20:23], v70, s[64:65] offset:32
	global_load_dwordx4 v[24:27], v70, s[64:65] offset:64
	global_load_dwordx4 v[28:31], v70, s[64:65] offset:96
	v_cvt_pk_f16_f32 v73, v118, v119
	v_cvt_pk_f16_f32 v72, v116, v117
	v_add_u32_e32 v76, v103, v105
	v_cvt_pk_f16_f32 v75, v122, v123
	v_cvt_pk_f16_f32 v74, v120, v121
	s_and_saveexec_b64 s[6:7], vcc
	s_cbranch_execz .LBB0_39
	v_lshl_or_b32 v71, v251, 12, v32
	v_add_u32_e32 v71, 0x18800, v71
	s_nop 0
	ds_write_b128 v71, v[0:3]
	ds_write_b128 v71, v[4:7] offset:1024
	ds_write_b128 v71, v[8:11] offset:2048
	ds_write_b128 v71, v[12:15] offset:3072
.LBB0_39:
	s_or_b64 exec, exec, s[6:7]
	s_waitcnt lgkmcnt(0)
	s_barrier
	ds_write2_b64 v76, v[72:73], v[74:75] offset1:34
	v_cvt_pk_f16_f32 v73, v126, v127
	v_cvt_pk_f16_f32 v72, v124, v125
	v_cvt_pk_f16_f32 v75, v130, v131
	v_cvt_pk_f16_f32 v74, v128, v129
	ds_write2_b64 v76, v[72:73], v[74:75] offset0:68 offset1:102
	v_cvt_pk_f16_f32 v73, v134, v135
	v_cvt_pk_f16_f32 v72, v132, v133
	v_cvt_pk_f16_f32 v75, v138, v139
	v_cvt_pk_f16_f32 v74, v136, v137
	ds_write2_b64 v76, v[72:73], v[74:75] offset0:136 offset1:170
	v_cvt_pk_f16_f32 v73, v142, v143
	v_cvt_pk_f16_f32 v72, v140, v141
	v_cvt_pk_f16_f32 v75, v146, v147
	v_cvt_pk_f16_f32 v74, v144, v145
	ds_write2_b64 v76, v[72:73], v[74:75] offset0:204 offset1:238
	s_and_saveexec_b64 s[6:7], s[0:1]
	s_cbranch_execz .LBB0_49
	v_mov_b32_e32 v215, 0
	v_add_u32_e32 v54, v224, v223
	ds_read_b128 v[34:37], v54
	s_movk_i32 s0, 0x110
	v_mad_u32_u24 v70, v220, s0, v223
	ds_read_b128 v[38:41], v70 offset:34816
	ds_read_b128 v[42:45], v54 offset:32
	ds_read_b128 v[46:49], v70 offset:34848
	v_lshl_or_b32 v32, v251, 12, v32
	v_add_u32_e32 v78, 0x18800, v32
	v_div_scale_f32 v82, s[0:1], s10, s10, 1.0
	v_rcp_f32_e32 v84, v82
	v_div_scale_f32 v83, vcc, 1.0, s10, 1.0
	s_waitcnt vmcnt(0) lgkmcnt(2)
	v_mfma_f32_32x32x16_f16 v[16:31], v[34:37], v[38:41], v[16:31]
	ds_read_b128 v[34:37], v54 offset:64
	ds_read_b128 v[38:41], v70 offset:34880
	s_waitcnt lgkmcnt(2)
	v_mfma_f32_32x32x16_f16 v[16:31], v[42:45], v[46:49], v[16:31]
	ds_read_b128 v[42:45], v54 offset:96
	ds_read_b128 v[46:49], v70 offset:34912
	s_waitcnt lgkmcnt(2)
	v_mfma_f32_32x32x16_f16 v[16:31], v[34:37], v[38:41], v[16:31]
	ds_read_b128 v[32:35], v54 offset:128
	ds_read_b128 v[36:39], v54 offset:160
	ds_read_b128 v[50:53], v54 offset:192
	ds_read_b128 v[54:57], v54 offset:224
	ds_read_b128 v[58:61], v70 offset:34944
	ds_read_b128 v[62:65], v70 offset:34976
	ds_read_b128 v[66:69], v70 offset:35008
	ds_read_b128 v[70:73], v70 offset:35040
	s_waitcnt lgkmcnt(8)
	v_mfma_f32_32x32x16_f16 v[16:31], v[42:45], v[46:49], v[16:31]
	ds_read_b128 v[40:43], v78
	ds_read_b128 v[44:47], v78 offset:1024
	ds_read_b128 v[74:77], v78 offset:2048
	ds_read_b128 v[78:81], v78 offset:3072
	v_fma_f32 v48, -v82, v84, 1.0
	v_fmac_f32_e32 v84, v48, v84
	v_mul_f32_e32 v48, v83, v84
	s_waitcnt lgkmcnt(7)
	v_mfma_f32_32x32x16_f16 v[16:31], v[32:35], v[58:61], v[16:31]
	s_waitcnt lgkmcnt(3)
	v_add_f32_e64 v32, v0, v40
	v_add_f32_e64 v33, v1, v41
	v_add_f32_e64 v0, v42, v2
	v_add_f32_e64 v1, v43, v3
	s_waitcnt lgkmcnt(2)
	v_pk_add_f32 v[2:3], v[4:5], v[44:45]
	v_pk_add_f32 v[4:5], v[46:47], v[6:7]
	s_waitcnt lgkmcnt(1)
	v_pk_add_f32 v[6:7], v[8:9], v[74:75]
	s_waitcnt lgkmcnt(0)
	v_pk_add_f32 v[8:9], v[12:13], v[78:79]
	v_fma_f32 v12, -v82, v48, v83
	v_mfma_f32_32x32x16_f16 v[16:31], v[36:39], v[62:65], v[16:31]
	v_fmac_f32_e32 v48, v12, v84
	v_cvt_pk_f16_f32 v2, v2, v3
	v_cvt_pk_f16_f32 v3, v4, v5
	v_cvt_pk_f16_f32 v1, v0, v1
	v_cvt_pk_f16_f32 v0, v32, v33
	v_fma_f32 v4, -v82, v48, v83
	v_div_fmas_f32 v4, v4, v84, v48
	v_mfma_f32_32x32x16_f16 v[16:31], v[50:53], v[66:69], v[16:31]
	v_add_f32_e64 v40, v76, v10
	v_add_f32_e64 v41, v77, v11
	v_add_f32_e64 v10, v80, v14
	v_add_f32_e64 v11, v81, v15
	v_div_fixup_f32 v4, v4, s10, 1.0
	v_cvt_pk_f16_f32 v34, v8, v9
	v_cvt_pk_f16_f32 v32, v6, v7
	v_cvt_pk_f16_f32 v35, v10, v11
	v_cvt_pk_f16_f32 v33, v40, v41
	v_mfma_f32_32x32x16_f16 v[16:31], v[54:57], v[70:73], v[16:31]
	s_andn2_b64 vcc, exec, s[8:9]
	s_nop 10
	v_mul_f32_e32 v8, v4, v16
	v_mul_f32_e32 v9, v4, v17
	v_mul_f32_e32 v5, v4, v18
	v_mul_f32_e32 v10, v4, v19
	v_mul_f32_e32 v6, v4, v20
	v_mul_f32_e32 v11, v4, v21
	v_mul_f32_e32 v7, v4, v22
	v_mul_f32_e32 v12, v4, v23
	v_mul_f32_e32 v16, v4, v24
	v_mul_f32_e32 v20, v4, v25
	v_mul_f32_e32 v17, v4, v26
	v_mul_f32_e32 v21, v4, v27
	v_mul_f32_e32 v18, v4, v28
	v_mul_f32_e32 v22, v4, v29
	v_mul_f32_e32 v19, v4, v30
	v_mul_f32_e32 v23, v4, v31
	v_cvt_pk_f16_f32 v7, v7, v12
	v_cvt_pk_f16_f32 v6, v6, v11
	v_cvt_pk_f16_f32 v5, v5, v10
	v_cvt_pk_f16_f32 v4, v8, v9
	v_cvt_pk_f16_f32 v19, v19, v23
	v_cvt_pk_f16_f32 v18, v18, v22
	v_mfma_f32_32x32x16_f16 v[0:15], v[0:3], v[4:7], 0
	v_cvt_pk_f16_f32 v17, v17, v21
	v_cvt_pk_f16_f32 v16, v16, v20
	s_nop 1
	v_mfma_f32_32x32x16_f16 v[0:15], v[32:35], v[16:19], v[0:15]
	s_cbranch_vccnz .LBB0_48
	v_lshlrev_b32_e32 v16, 7, v220
	v_lshl_or_b32 v16, v251, 12, v16
	v_mov_b32_e32 v17, v215
	s_add_i32 s33, s33, s46
	v_lshlrev_b32_e32 v22, 2, v214
	v_lshl_add_u64 v[16:17], v[16:17], 2, s[44:45]
	v_add_u32_e32 v18, s33, v214
	s_mov_b64 s[0:1], 0
	s_movk_i32 s10, 0x3fd
	v_mov_b32_e32 v23, v215
	s_branch .LBB0_43
